# all MoE weight conversion (layers 0-3) inside attention phase queues; prologue converts no expert weights
# speedup vs baseline: 1.0537x; 1.0137x over previous
.LBB0_20:
	s_mov_b32 s2, 0x83fef803
	v_mul_hi_i32 v2, v1, s2
	v_add_u32_e32 v2, v2, v1
	v_lshrrev_b32_e32 v8, 31, v2
	v_ashrrev_i32_e32 v2, 13, v2
	v_add_u32_e32 v8, v2, v8
	v_mul_i32_i24_e32 v12, 0x3e10, v8
	v_sub_u32_e32 v2, v1, v12
	s_movk_i32 s2, 0xa8f
	v_cmp_lt_i32_e32 vcc, s2, v2
	s_and_saveexec_b64 s[2:3], vcc
	s_xor_b64 s[24:25], exec, s[2:3]
	s_cbranch_execz .LBB0_35
	s_movk_i32 s2, 0xc0f
	v_cmp_lt_u32_e32 vcc, s2, v2
	s_and_saveexec_b64 s[2:3], vcc
	s_xor_b64 s[26:27], exec, s[2:3]
	s_cbranch_execz .LBB0_32
	s_movk_i32 s2, 0xe0f
	v_cmp_lt_u32_e32 vcc, s2, v2
	s_and_saveexec_b64 s[2:3], vcc
	s_xor_b64 s[28:29], exec, s[2:3]
	s_cbranch_execz .LBB0_29
	s_movk_i32 s2, 0
	v_cmp_gt_i32_e32 vcc, s2, v1
	s_movk_i32 s2, 0x3e0f
	v_cmp_lt_u32_e64 s[2:3], s2, v2
	s_or_b64 s[30:31], vcc, s[2:3]
	s_and_saveexec_b64 s[2:3], s[30:31]
	s_cbranch_execz .LBB0_28
	v_add_u32_e32 v11, 0xfffff1f0, v2
	s_movk_i32 s30, 0x1fff
	v_cmp_lt_u32_e32 vcc, s30, v11
	v_lshlrev_b32_e32 v10, 2, v0
	s_and_saveexec_b64 s[30:31], vcc
	s_xor_b64 s[30:31], exec, s[30:31]
	s_cbranch_execz .LBB0_26
	s_load_dwordx2 s[34:35], s[6:7], 0x70
	v_add_u32_e32 v2, 0xffffd1f0, v2
	v_lshrrev_b32_e32 v2, 7, v2
	v_ashrrev_i32_e32 v9, 31, v8
	v_lshlrev_b64 v[12:13], 20, v[2:3]
	v_lshlrev_b64 v[8:9], 25, v[8:9]
	v_lshlrev_b32_e32 v2, 3, v11
	v_lshl_add_u64 v[8:9], v[12:13], 0, v[8:9]
	v_and_b32_e32 v2, 0x380, v2
	v_lshlrev_b32_e32 v11, 6, v11
	s_waitcnt lgkmcnt(0)
	v_lshl_add_u64 v[12:13], v[8:9], 2, s[34:35]
	v_and_b32_e32 v79, 0x3c0, v11
	v_lshlrev_b32_e32 v14, 12, v2
	v_mov_b32_e32 v15, v3
	v_lshl_add_u64 v[12:13], v[12:13], 0, v[14:15]
	v_lshlrev_b32_e32 v14, 2, v79
	v_lshl_add_u64 v[12:13], v[12:13], 0, v[14:15]
	v_mov_b32_e32 v11, v3
	v_lshl_add_u64 v[10:11], v[12:13], 0, v[10:11]
	s_mov_b32 s34, 0x10000
	v_add_co_u32_e32 v12, vcc, s34, v10
	s_mov_b32 s34, 0xe000
	s_nop 0
	v_addc_co_u32_e32 v13, vcc, 0, v11, vcc
	v_add_co_u32_e32 v14, vcc, s34, v10
	s_mov_b32 s34, 0xd000
	s_nop 0
	v_addc_co_u32_e32 v15, vcc, 0, v11, vcc
	global_load_dword v80, v[12:13], off offset:-4096 nt
	global_load_dword v81, v[14:15], off nt
	v_add_co_u32_e32 v14, vcc, s34, v10
	s_mov_b32 s34, 0xc000
	s_nop 0
	v_addc_co_u32_e32 v15, vcc, 0, v11, vcc
	global_load_dword v82, v[14:15], off nt
	v_add_co_u32_e32 v14, vcc, s34, v10
	s_mov_b32 s34, 0xb000
	s_nop 0
	v_addc_co_u32_e32 v15, vcc, 0, v11, vcc
	global_load_dword v83, v[14:15], off nt
	v_add_co_u32_e32 v14, vcc, s34, v10
	s_mov_b32 s34, 0xa000
	s_nop 0
	v_addc_co_u32_e32 v15, vcc, 0, v11, vcc
	global_load_dword v84, v[14:15], off nt
	v_add_co_u32_e32 v14, vcc, s34, v10
	s_mov_b32 s34, 0x9000
	s_nop 0
	v_addc_co_u32_e32 v15, vcc, 0, v11, vcc
	global_load_dword v85, v[14:15], off nt
	v_add_co_u32_e32 v14, vcc, s34, v10
	s_mov_b32 s34, 0x8000
	s_nop 0
	v_addc_co_u32_e32 v15, vcc, 0, v11, vcc
	global_load_dword v87, v[14:15], off nt
	v_add_co_u32_e32 v14, vcc, s34, v10
	s_movk_i32 s34, 0x7000
	s_nop 0
	v_addc_co_u32_e32 v15, vcc, 0, v11, vcc
	global_load_dword v88, v[14:15], off nt
	v_add_co_u32_e32 v14, vcc, s34, v10
	s_movk_i32 s34, 0x6000
	s_nop 0
	v_addc_co_u32_e32 v15, vcc, 0, v11, vcc
	global_load_dword v92, v[14:15], off nt
	v_add_co_u32_e32 v14, vcc, s34, v10
	s_movk_i32 s34, 0x5000
	s_nop 0
	v_addc_co_u32_e32 v15, vcc, 0, v11, vcc
	global_load_dword v97, v[14:15], off nt
	v_add_co_u32_e32 v14, vcc, s34, v10
	s_movk_i32 s34, 0x4000
	s_nop 0
	v_addc_co_u32_e32 v15, vcc, 0, v11, vcc
	global_load_dword v100, v[14:15], off nt
	v_add_co_u32_e32 v14, vcc, s34, v10
	s_movk_i32 s34, 0x3000
	s_nop 0
	v_addc_co_u32_e32 v15, vcc, 0, v11, vcc
	global_load_dword v105, v[14:15], off nt
	v_add_co_u32_e32 v14, vcc, s34, v10
	s_movk_i32 s34, 0x2000
	s_nop 0
	v_addc_co_u32_e32 v15, vcc, 0, v11, vcc
	global_load_dword v112, v[14:15], off nt
	v_add_co_u32_e32 v14, vcc, s34, v10
	s_movk_i32 s34, 0x1000
	s_nop 0
	v_addc_co_u32_e32 v15, vcc, 0, v11, vcc
	global_load_dword v114, v[14:15], off nt
	v_add_co_u32_e32 v14, vcc, s34, v10
	s_mov_b32 s34, 0x20000
	s_nop 0
	v_addc_co_u32_e32 v15, vcc, 0, v11, vcc
	v_add_co_u32_e32 v122, vcc, s34, v10
	s_mov_b32 s34, 0x1e000
	s_nop 0
	v_addc_co_u32_e32 v123, vcc, 0, v11, vcc
	global_load_dword v120, v[14:15], off nt
	global_load_dword v124, v[10:11], off nt
	v_add_co_u32_e32 v14, vcc, s34, v10
	s_mov_b32 s34, 0x1d000
	s_nop 0
	v_addc_co_u32_e32 v15, vcc, 0, v11, vcc
	global_load_dword v86, v[122:123], off offset:-4096 nt
	global_load_dword v89, v[14:15], off nt
	v_add_co_u32_e32 v14, vcc, s34, v10
	s_mov_b32 s34, 0x1c000
	s_nop 0
	v_addc_co_u32_e32 v15, vcc, 0, v11, vcc
	global_load_dword v90, v[14:15], off nt
	v_add_co_u32_e32 v14, vcc, s34, v10
	s_mov_b32 s34, 0x1b000
	s_nop 0
	v_addc_co_u32_e32 v15, vcc, 0, v11, vcc
	global_load_dword v91, v[14:15], off nt
	v_add_co_u32_e32 v14, vcc, s34, v10
	s_mov_b32 s34, 0x1a000
	s_nop 0
	v_addc_co_u32_e32 v15, vcc, 0, v11, vcc
	global_load_dword v95, v[14:15], off nt
	v_add_co_u32_e32 v14, vcc, s34, v10
	s_mov_b32 s34, 0x19000
	s_nop 0
	v_addc_co_u32_e32 v15, vcc, 0, v11, vcc
	global_load_dword v99, v[14:15], off nt
	v_add_co_u32_e32 v14, vcc, s34, v10
	s_mov_b32 s34, 0x18000
	s_nop 0
	v_addc_co_u32_e32 v15, vcc, 0, v11, vcc
	global_load_dword v104, v[14:15], off nt
	v_add_co_u32_e32 v14, vcc, s34, v10
	s_mov_b32 s34, 0x17000
	s_nop 0
	v_addc_co_u32_e32 v15, vcc, 0, v11, vcc
	global_load_dword v110, v[14:15], off nt
	v_add_co_u32_e32 v14, vcc, s34, v10
	s_mov_b32 s34, 0x16000
	s_nop 0
	v_addc_co_u32_e32 v15, vcc, 0, v11, vcc
	global_load_dword v121, v[14:15], off nt
	v_add_co_u32_e32 v14, vcc, s34, v10
	s_mov_b32 s34, 0x15000
	s_nop 0
	v_addc_co_u32_e32 v15, vcc, 0, v11, vcc
	global_load_dword v126, v[14:15], off nt
	v_add_co_u32_e32 v14, vcc, s34, v10
	s_mov_b32 s34, 0x14000
	s_nop 0
	v_addc_co_u32_e32 v15, vcc, 0, v11, vcc
	global_load_dword v130, v[14:15], off nt
	v_add_co_u32_e32 v14, vcc, s34, v10
	s_mov_b32 s34, 0x13000
	s_nop 0
	v_addc_co_u32_e32 v15, vcc, 0, v11, vcc
	global_load_dword v133, v[14:15], off nt
	v_add_co_u32_e32 v14, vcc, s34, v10
	s_mov_b32 s34, 0x12000
	s_nop 0
	v_addc_co_u32_e32 v15, vcc, 0, v11, vcc
	global_load_dword v137, v[14:15], off nt
	v_add_co_u32_e32 v14, vcc, s34, v10
	s_mov_b32 s34, 0x11000
	s_nop 0
	v_addc_co_u32_e32 v15, vcc, 0, v11, vcc
	global_load_dword v140, v[14:15], off nt
	v_add_co_u32_e32 v14, vcc, s34, v10
	s_mov_b32 s34, 0x2e000
	s_nop 0
	v_addc_co_u32_e32 v15, vcc, 0, v11, vcc
	global_load_dword v141, v[14:15], off nt
	global_load_dword v142, v[12:13], off nt
	v_add_co_u32_e32 v14, vcc, s79, v10
	v_mov_b32_e32 v206, v3
	s_nop 0
	v_addc_co_u32_e32 v15, vcc, 0, v11, vcc
	v_add_co_u32_e32 v12, vcc, s34, v10
	s_mov_b32 s34, 0x2d000
	s_nop 0
	v_addc_co_u32_e32 v13, vcc, 0, v11, vcc
	global_load_dword v102, v[14:15], off offset:-4096 nt
	global_load_dword v106, v[12:13], off nt
	v_add_co_u32_e32 v12, vcc, s34, v10
	s_mov_b32 s34, 0x2c000
	s_nop 0
	v_addc_co_u32_e32 v13, vcc, 0, v11, vcc
	global_load_dword v109, v[12:13], off nt
	v_add_co_u32_e32 v12, vcc, s34, v10
	s_mov_b32 s34, 0x2b000
	s_nop 0
	v_addc_co_u32_e32 v13, vcc, 0, v11, vcc
	global_load_dword v111, v[12:13], off nt
	v_add_co_u32_e32 v12, vcc, s34, v10
	s_mov_b32 s34, 0x2a000
	s_nop 0
	v_addc_co_u32_e32 v13, vcc, 0, v11, vcc
	global_load_dword v113, v[12:13], off nt
	v_add_co_u32_e32 v12, vcc, s34, v10
	s_mov_b32 s34, 0x29000
	s_nop 0
	v_addc_co_u32_e32 v13, vcc, 0, v11, vcc
	global_load_dword v115, v[12:13], off nt
	v_add_co_u32_e32 v12, vcc, s34, v10
	s_mov_b32 s34, 0x28000
	s_nop 0
	v_addc_co_u32_e32 v13, vcc, 0, v11, vcc
	global_load_dword v116, v[12:13], off nt
	v_add_co_u32_e32 v12, vcc, s34, v10
	s_mov_b32 s34, 0x27000
	s_nop 0
	v_addc_co_u32_e32 v13, vcc, 0, v11, vcc
	global_load_dword v119, v[12:13], off nt
	v_add_co_u32_e32 v12, vcc, s34, v10
	s_mov_b32 s34, 0x26000
	s_nop 0
	v_addc_co_u32_e32 v13, vcc, 0, v11, vcc
	global_load_dword v128, v[12:13], off nt
	v_add_co_u32_e32 v12, vcc, s34, v10
	s_mov_b32 s34, 0x25000
	s_nop 0
	v_addc_co_u32_e32 v13, vcc, 0, v11, vcc
	global_load_dword v131, v[12:13], off nt
	v_add_co_u32_e32 v12, vcc, s34, v10
	s_mov_b32 s34, 0x24000
	s_nop 0
	v_addc_co_u32_e32 v13, vcc, 0, v11, vcc
	global_load_dword v132, v[12:13], off nt
	v_add_co_u32_e32 v12, vcc, s34, v10
	s_mov_b32 s34, 0x23000
	s_nop 0
	v_addc_co_u32_e32 v13, vcc, 0, v11, vcc
	global_load_dword v134, v[12:13], off nt
	v_add_co_u32_e32 v12, vcc, s34, v10
	s_mov_b32 s34, 0x21000
	s_nop 0
	v_addc_co_u32_e32 v13, vcc, 0, v11, vcc
	global_load_dword v135, v[12:13], off nt
	v_add_co_u32_e32 v12, vcc, s71, v10
	v_mov_b32_e32 v207, v3
	s_nop 0
	v_addc_co_u32_e32 v13, vcc, 0, v11, vcc
	global_load_dword v136, v[12:13], off nt
	v_add_co_u32_e32 v12, vcc, s34, v10
	s_mov_b32 s34, 0x3d000
	s_nop 0
	v_addc_co_u32_e32 v13, vcc, 0, v11, vcc
	global_load_dword v138, v[12:13], off nt
	global_load_dword v139, v[122:123], off nt
	v_add_co_u32_e32 v12, vcc, s87, v10
	v_lshl_add_u64 v[8:9], s[10:11], 0, v[8:9]
	s_nop 0
	v_addc_co_u32_e32 v13, vcc, 0, v11, vcc
	v_add_co_u32_e32 v122, vcc, s72, v10
	global_load_dword v93, v[12:13], off offset:-4096 nt
	s_nop 0
	v_addc_co_u32_e32 v123, vcc, 0, v11, vcc
	global_load_dword v94, v[122:123], off nt
	v_add_co_u32_e32 v122, vcc, s34, v10
	s_mov_b32 s34, 0x3b000
	s_nop 0
	v_addc_co_u32_e32 v123, vcc, 0, v11, vcc
	global_load_dword v96, v[122:123], off nt
	v_add_co_u32_e32 v122, vcc, s73, v10
	v_lshl_add_u64 v[8:9], v[8:9], 0, v[2:3]
	s_nop 0
	v_addc_co_u32_e32 v123, vcc, 0, v11, vcc
	global_load_dword v98, v[122:123], off nt
	v_add_co_u32_e32 v122, vcc, s34, v10
	s_mov_b32 s34, 0x39000
	s_nop 0
	v_addc_co_u32_e32 v123, vcc, 0, v11, vcc
	global_load_dword v101, v[122:123], off nt
	v_add_co_u32_e32 v122, vcc, s74, v10
	v_or_b32_e32 v2, v79, v18
	s_nop 0
	v_addc_co_u32_e32 v123, vcc, 0, v11, vcc
	global_load_dword v103, v[122:123], off nt
	v_add_co_u32_e32 v122, vcc, s34, v10
	s_mov_b32 s34, 0x37000
	s_nop 0
	v_addc_co_u32_e32 v123, vcc, 0, v11, vcc
	global_load_dword v107, v[122:123], off nt
	v_add_co_u32_e32 v122, vcc, s75, v10
	v_lshlrev_b32_e32 v2, 10, v2
	s_nop 0
	v_addc_co_u32_e32 v123, vcc, 0, v11, vcc
	global_load_dword v108, v[122:123], off nt
	v_add_co_u32_e32 v122, vcc, s34, v10
	s_mov_b32 s34, 0x35000
	s_nop 0
	v_addc_co_u32_e32 v123, vcc, 0, v11, vcc
	global_load_dword v117, v[122:123], off nt
	v_add_co_u32_e32 v122, vcc, s76, v10
	s_nop 1
	v_addc_co_u32_e32 v123, vcc, 0, v11, vcc
	global_load_dword v118, v[122:123], off nt
	v_add_co_u32_e32 v122, vcc, s34, v10
	s_mov_b32 s34, 0x33000
	s_nop 0
	v_addc_co_u32_e32 v123, vcc, 0, v11, vcc
	v_add_co_u32_e32 v144, vcc, s77, v10
	global_load_dword v122, v[122:123], off nt
	s_nop 0
	v_addc_co_u32_e32 v145, vcc, 0, v11, vcc
	global_load_dword v123, v[144:145], off nt
	v_add_co_u32_e32 v144, vcc, s34, v10
	s_mov_b32 s34, 0x31000
	s_nop 0
	v_addc_co_u32_e32 v145, vcc, 0, v11, vcc
	global_load_dword v125, v[144:145], off nt
	v_add_co_u32_e32 v144, vcc, s78, v10
	s_nop 1
	v_addc_co_u32_e32 v145, vcc, 0, v11, vcc
	global_load_dword v127, v[144:145], off nt
	v_add_co_u32_e32 v144, vcc, s34, v10
	s_mov_b32 s34, 0x4d000
	s_nop 0
	v_addc_co_u32_e32 v145, vcc, 0, v11, vcc
	v_add_co_u32_e32 v176, vcc, s95, v10
	global_load_dword v129, v[144:145], off nt
	s_nop 0
	global_load_dword v145, v[14:15], off nt
	v_addc_co_u32_e32 v177, vcc, 0, v11, vcc
	v_add_co_u32_e32 v146, vcc, s80, v10
	global_load_dword v14, v[176:177], off offset:-4096 nt
	s_nop 0
	v_addc_co_u32_e32 v147, vcc, 0, v11, vcc
	global_load_dword v15, v[146:147], off nt
	v_add_co_u32_e32 v146, vcc, s34, v10
	s_mov_b32 s34, 0x4b000
	s_nop 0
	v_addc_co_u32_e32 v147, vcc, 0, v11, vcc
	global_load_dword v143, v[146:147], off nt
	v_add_co_u32_e32 v146, vcc, s81, v10
	s_nop 1
	v_addc_co_u32_e32 v147, vcc, 0, v11, vcc
	global_load_dword v144, v[146:147], off nt
	v_add_co_u32_e32 v146, vcc, s34, v10
	s_mov_b32 s34, 0x49000
	s_nop 0
	v_addc_co_u32_e32 v147, vcc, 0, v11, vcc
	v_add_co_u32_e32 v148, vcc, s82, v10
	global_load_dword v146, v[146:147], off nt
	s_nop 0
	v_addc_co_u32_e32 v149, vcc, 0, v11, vcc
	global_load_dword v147, v[148:149], off nt
	v_add_co_u32_e32 v148, vcc, s34, v10
	s_mov_b32 s34, 0x47000
	s_nop 0
	v_addc_co_u32_e32 v149, vcc, 0, v11, vcc
	global_load_dword v150, v[148:149], off nt
	v_add_co_u32_e32 v148, vcc, s83, v10
	s_nop 1
	v_addc_co_u32_e32 v149, vcc, 0, v11, vcc
	global_load_dword v153, v[148:149], off nt
	v_add_co_u32_e32 v148, vcc, s34, v10
	s_mov_b32 s34, 0x45000
	s_nop 0
	v_addc_co_u32_e32 v149, vcc, 0, v11, vcc
	global_load_dword v158, v[148:149], off nt
	v_add_co_u32_e32 v148, vcc, s84, v10
	s_nop 1
	v_addc_co_u32_e32 v149, vcc, 0, v11, vcc
	global_load_dword v161, v[148:149], off nt
	v_add_co_u32_e32 v148, vcc, s34, v10
	s_mov_b32 s34, 0x43000
	s_nop 0
	v_addc_co_u32_e32 v149, vcc, 0, v11, vcc
	global_load_dword v167, v[148:149], off nt
	v_add_co_u32_e32 v148, vcc, s85, v10
	s_nop 1
	v_addc_co_u32_e32 v149, vcc, 0, v11, vcc
	global_load_dword v170, v[148:149], off nt
	v_add_co_u32_e32 v148, vcc, s34, v10
	s_mov_b32 s34, 0x41000
	s_nop 0
	v_addc_co_u32_e32 v149, vcc, 0, v11, vcc
	global_load_dword v181, v[148:149], off nt
	v_add_co_u32_e32 v148, vcc, s86, v10
	s_nop 1
	v_addc_co_u32_e32 v149, vcc, 0, v11, vcc
	global_load_dword v183, v[148:149], off nt
	v_add_co_u32_e32 v148, vcc, s34, v10
	s_mov_b32 s34, 0x5d000
	s_nop 0
	v_addc_co_u32_e32 v149, vcc, 0, v11, vcc
	v_add_co_u32_e32 v192, vcc, s54, v10
	global_load_dword v186, v[148:149], off nt
	global_load_dword v188, v[12:13], off nt
	v_addc_co_u32_e32 v193, vcc, 0, v11, vcc
	v_add_co_u32_e32 v12, vcc, s88, v10
	global_load_dword v148, v[192:193], off offset:-4096 nt
	s_nop 0
	v_addc_co_u32_e32 v13, vcc, 0, v11, vcc
	global_load_dword v149, v[12:13], off nt
	v_add_co_u32_e32 v12, vcc, s34, v10
	s_mov_b32 s34, 0x5b000
	s_nop 0
	v_addc_co_u32_e32 v13, vcc, 0, v11, vcc
	global_load_dword v151, v[12:13], off nt
	v_add_co_u32_e32 v12, vcc, s89, v10
	s_nop 1
	v_addc_co_u32_e32 v13, vcc, 0, v11, vcc
	global_load_dword v152, v[12:13], off nt
	v_add_co_u32_e32 v12, vcc, s34, v10
	s_mov_b32 s34, 0x59000
	s_nop 0
	v_addc_co_u32_e32 v13, vcc, 0, v11, vcc
	global_load_dword v154, v[12:13], off nt
	v_add_co_u32_e32 v12, vcc, s90, v10
	s_nop 1
	v_addc_co_u32_e32 v13, vcc, 0, v11, vcc
	global_load_dword v155, v[12:13], off nt
	v_add_co_u32_e32 v12, vcc, s34, v10
	s_mov_b32 s34, 0x57000
	s_nop 0
	v_addc_co_u32_e32 v13, vcc, 0, v11, vcc
	global_load_dword v156, v[12:13], off nt
	v_add_co_u32_e32 v12, vcc, s91, v10
	s_nop 1
	v_addc_co_u32_e32 v13, vcc, 0, v11, vcc
	global_load_dword v157, v[12:13], off nt
	v_add_co_u32_e32 v12, vcc, s34, v10
	s_mov_b32 s34, 0x55000
	s_nop 0
	v_addc_co_u32_e32 v13, vcc, 0, v11, vcc
	global_load_dword v162, v[12:13], off nt
	v_add_co_u32_e32 v12, vcc, s92, v10
	s_nop 1
	v_addc_co_u32_e32 v13, vcc, 0, v11, vcc
	global_load_dword v164, v[12:13], off nt
	v_add_co_u32_e32 v12, vcc, s34, v10
	s_mov_b32 s34, 0x53000
	s_nop 0
	v_addc_co_u32_e32 v13, vcc, 0, v11, vcc
	global_load_dword v166, v[12:13], off nt
	v_add_co_u32_e32 v12, vcc, s93, v10
	s_nop 1
	v_addc_co_u32_e32 v13, vcc, 0, v11, vcc
	global_load_dword v168, v[12:13], off nt
	v_add_co_u32_e32 v12, vcc, s34, v10
	s_mov_b32 s34, 0x51000
	s_nop 0
	v_addc_co_u32_e32 v13, vcc, 0, v11, vcc
	global_load_dword v172, v[12:13], off nt
	v_add_co_u32_e32 v12, vcc, s94, v10
	s_nop 1
	v_addc_co_u32_e32 v13, vcc, 0, v11, vcc
	global_load_dword v175, v[12:13], off nt
	v_add_co_u32_e32 v12, vcc, s34, v10
	s_mov_b32 s34, 0x6d000
	s_nop 0
	v_addc_co_u32_e32 v13, vcc, 0, v11, vcc
	global_load_dword v178, v[12:13], off nt
	global_load_dword v179, v[176:177], off nt
	v_add_co_u32_e32 v12, vcc, s62, v10
	s_nop 1
	v_addc_co_u32_e32 v13, vcc, 0, v11, vcc
	v_add_co_u32_e32 v176, vcc, s97, v10
	global_load_dword v173, v[12:13], off offset:-4096 nt
	s_nop 0
	v_addc_co_u32_e32 v177, vcc, 0, v11, vcc
	v_add_co_u32_e32 v184, vcc, s34, v10
	global_load_dword v176, v[176:177], off nt
	s_nop 0
	v_addc_co_u32_e32 v185, vcc, 0, v11, vcc
	global_load_dword v180, v[184:185], off nt
	v_add_co_u32_e32 v184, vcc, s69, v10
	s_mov_b32 s34, 0x6b000
	s_nop 0
	v_addc_co_u32_e32 v185, vcc, 0, v11, vcc
	global_load_dword v182, v[184:185], off nt
	v_add_co_u32_e32 v184, vcc, s34, v10
	s_mov_b32 s34, 0x69000
	s_nop 0
	v_addc_co_u32_e32 v185, vcc, 0, v11, vcc
	v_add_co_u32_e32 v190, vcc, s49, v10
	global_load_dword v184, v[184:185], off nt
	s_nop 0
	v_addc_co_u32_e32 v191, vcc, 0, v11, vcc
	global_load_dword v185, v[190:191], off nt
	v_add_co_u32_e32 v190, vcc, s34, v10
	s_mov_b32 s34, 0x67000
	s_nop 0
	v_addc_co_u32_e32 v191, vcc, 0, v11, vcc
	global_load_dword v189, v[190:191], off nt
	v_add_co_u32_e32 v190, vcc, s50, v10
	s_nop 1
	v_addc_co_u32_e32 v191, vcc, 0, v11, vcc
	v_add_co_u32_e32 v194, vcc, s34, v10
	global_load_dword v191, v[190:191], off nt
	s_nop 0
	v_addc_co_u32_e32 v195, vcc, 0, v11, vcc
	global_load_dword v196, v[194:195], off nt
	v_add_co_u32_e32 v194, vcc, s51, v10
	s_mov_b32 s34, 0x65000
	s_nop 0
	v_addc_co_u32_e32 v195, vcc, 0, v11, vcc
	global_load_dword v197, v[194:195], off nt
	v_add_co_u32_e32 v194, vcc, s34, v10
	s_mov_b32 s34, 0x63000
	s_nop 0
	v_addc_co_u32_e32 v195, vcc, 0, v11, vcc
	global_load_dword v198, v[194:195], off nt
	v_add_co_u32_e32 v194, vcc, s52, v10
	s_nop 1
	v_addc_co_u32_e32 v195, vcc, 0, v11, vcc
	global_load_dword v199, v[194:195], off nt
	v_add_co_u32_e32 v194, vcc, s34, v10
	s_mov_b32 s34, 0x61000
	s_nop 0
	v_addc_co_u32_e32 v195, vcc, 0, v11, vcc
	global_load_dword v200, v[194:195], off nt
	v_add_co_u32_e32 v194, vcc, s53, v10
	s_nop 1
	v_addc_co_u32_e32 v195, vcc, 0, v11, vcc
	global_load_dword v201, v[194:195], off nt
	v_add_co_u32_e32 v194, vcc, s34, v10
	s_mov_b32 s34, 0x7f000
	s_nop 0
	v_addc_co_u32_e32 v195, vcc, 0, v11, vcc
	global_load_dword v202, v[194:195], off nt
	global_load_dword v203, v[192:193], off nt
	v_add_co_u32_e32 v192, vcc, s34, v10
	s_mov_b32 s34, 0x7d000
	s_nop 0
	v_addc_co_u32_e32 v193, vcc, 0, v11, vcc
	global_load_dword v159, v[192:193], off nt
	v_add_co_u32_e32 v192, vcc, s55, v10
	s_nop 1
	v_addc_co_u32_e32 v193, vcc, 0, v11, vcc
	global_load_dword v160, v[192:193], off nt
	v_add_co_u32_e32 v192, vcc, s34, v10
	s_mov_b32 s34, 0x7b000
	s_nop 0
	v_addc_co_u32_e32 v193, vcc, 0, v11, vcc
	global_load_dword v163, v[192:193], off nt
	v_add_co_u32_e32 v192, vcc, s56, v10
	s_nop 1
	v_addc_co_u32_e32 v193, vcc, 0, v11, vcc
	global_load_dword v165, v[192:193], off nt
	v_add_co_u32_e32 v192, vcc, s34, v10
	s_mov_b32 s34, 0x79000
	s_nop 0
	v_addc_co_u32_e32 v193, vcc, 0, v11, vcc
	global_load_dword v169, v[192:193], off nt
	v_add_co_u32_e32 v192, vcc, s57, v10
	s_nop 1
	v_addc_co_u32_e32 v193, vcc, 0, v11, vcc
	global_load_dword v171, v[192:193], off nt
	v_add_co_u32_e32 v192, vcc, s34, v10
	s_mov_b32 s34, 0x77000
	s_nop 0
	v_addc_co_u32_e32 v193, vcc, 0, v11, vcc
	global_load_dword v174, v[192:193], off nt
	v_add_co_u32_e32 v192, vcc, s58, v10
	s_nop 1
	v_addc_co_u32_e32 v193, vcc, 0, v11, vcc
	global_load_dword v177, v[192:193], off nt
	v_add_co_u32_e32 v192, vcc, s34, v10
	s_mov_b32 s34, 0x75000
	s_nop 0
	v_addc_co_u32_e32 v193, vcc, 0, v11, vcc
	global_load_dword v187, v[192:193], off nt
	v_add_co_u32_e32 v192, vcc, s59, v10
	s_nop 1
	v_addc_co_u32_e32 v193, vcc, 0, v11, vcc
	global_load_dword v190, v[192:193], off nt
	v_add_co_u32_e32 v192, vcc, s34, v10
	s_mov_b32 s34, 0x73000
	s_nop 0
	v_addc_co_u32_e32 v193, vcc, 0, v11, vcc
	v_add_co_u32_e32 v194, vcc, s60, v10
	global_load_dword v192, v[192:193], off nt
	s_nop 0
	v_addc_co_u32_e32 v195, vcc, 0, v11, vcc
	global_load_dword v193, v[194:195], off nt
	v_add_co_u32_e32 v194, vcc, s34, v10
	s_mov_b32 s34, 0x71000
	s_nop 0
	v_addc_co_u32_e32 v195, vcc, 0, v11, vcc
	v_add_co_u32_e32 v204, vcc, s61, v10
	global_load_dword v194, v[194:195], off nt
	s_nop 0
	v_addc_co_u32_e32 v205, vcc, 0, v11, vcc
	v_add_co_u32_e32 v10, vcc, s34, v10
	global_load_dword v195, v[204:205], off nt
	s_nop 0
	v_addc_co_u32_e32 v11, vcc, 0, v11, vcc
	global_load_dword v10, v[10:11], off nt
	s_nop 0
	global_load_dword v11, v[12:13], off nt
	s_waitcnt vmcnt(62)
	v_mov_b32_e32 v204, v3
	v_mul_f32_e32 v12, 0x42800000, v124
	v_mul_f32_e32 v13, 0x42800000, v120
	v_cvt_pk_fp8_f32 v204, v12, v13
	v_mul_f32_e32 v12, 0x42800000, v105
	v_mul_f32_e32 v13, 0x42800000, v100
	v_mov_b32_e32 v205, v3
	v_cvt_pk_fp8_f32 v205, v12, v13
	v_mul_f32_e32 v12, 0x42800000, v88
	v_mul_f32_e32 v13, 0x42800000, v87
	v_cvt_pk_fp8_f32 v206, v12, v13
	v_mul_f32_e32 v12, 0x42800000, v83
	v_mul_f32_e32 v13, 0x42800000, v82
	v_cvt_pk_fp8_f32 v207, v12, v13
	v_mul_f32_e32 v81, 0x42800000, v81
	v_mul_f32_e32 v80, 0x42800000, v80
	v_cvt_pk_fp8_f32 v207, v81, v80 op_sel:[0,0,1]
	v_mul_f32_e32 v13, 0x42800000, v142
	v_mul_f32_e32 v81, 0x42800000, v141
	v_mov_b32_e32 v80, v3
	v_cvt_pk_fp8_f32 v80, v13, v81
	v_mul_f32_e32 v82, 0x42800000, v140
	v_mul_f32_e32 v83, 0x42800000, v137
	v_mul_f32_e32 v13, 0x42800000, v133
	v_cvt_pk_fp8_f32 v80, v82, v83 op_sel:[0,0,1]
	v_mul_f32_e32 v82, 0x42800000, v130
	v_mov_b32_e32 v81, v3
	v_cvt_pk_fp8_f32 v81, v13, v82
	v_mul_f32_e32 v85, 0x42800000, v85
	v_mul_f32_e32 v84, 0x42800000, v84
	v_cvt_pk_fp8_f32 v206, v85, v84 op_sel:[0,0,1]
	v_mul_f32_e32 v83, 0x42800000, v126
	v_mul_f32_e32 v84, 0x42800000, v121
	v_cvt_pk_fp8_f32 v81, v83, v84 op_sel:[0,0,1]
	v_mul_f32_e32 v13, 0x42800000, v110
	v_mul_f32_e32 v83, 0x42800000, v104
	v_mov_b32_e32 v82, v3
	v_cvt_pk_fp8_f32 v82, v13, v83
	v_mul_f32_e32 v84, 0x42800000, v99
	v_mul_f32_e32 v85, 0x42800000, v95
	v_mul_f32_e32 v13, 0x42800000, v91
	v_cvt_pk_fp8_f32 v82, v84, v85 op_sel:[0,0,1]
	v_mul_f32_e32 v84, 0x42800000, v90
	v_mov_b32_e32 v83, v3
	v_cvt_pk_fp8_f32 v83, v13, v84
	v_mul_f32_e32 v85, 0x42800000, v89
	v_mul_f32_e32 v86, 0x42800000, v86
	v_add_u32_e32 v12, v16, v17
	v_cvt_pk_fp8_f32 v83, v85, v86 op_sel:[0,0,1]
	s_waitcnt vmcnt(48)
	s_waitcnt vmcnt(32)
	s_waitcnt vmcnt(16)
	s_waitcnt vmcnt(0)
	ds_write_b128 v12, v[80:83] offset:16
	v_mul_f32_e32 v13, 0x42800000, v139
	v_mul_f32_e32 v81, 0x42800000, v138
	v_mov_b32_e32 v80, v3
	v_cvt_pk_fp8_f32 v80, v13, v81
	v_mul_f32_e32 v82, 0x42800000, v136
	v_mul_f32_e32 v83, 0x42800000, v135
	v_mul_f32_e32 v13, 0x42800000, v134
	v_cvt_pk_fp8_f32 v80, v82, v83 op_sel:[0,0,1]
	v_mul_f32_e32 v82, 0x42800000, v132
	v_mov_b32_e32 v81, v3
	v_cvt_pk_fp8_f32 v81, v13, v82
	v_mul_f32_e32 v83, 0x42800000, v131
	v_mul_f32_e32 v84, 0x42800000, v128
	v_mul_f32_e32 v13, 0x42800000, v119
	v_cvt_pk_fp8_f32 v81, v83, v84 op_sel:[0,0,1]
	v_mul_f32_e32 v83, 0x42800000, v116
	v_mov_b32_e32 v82, v3
	v_cvt_pk_fp8_f32 v82, v13, v83
	v_mul_f32_e32 v84, 0x42800000, v115
	v_mul_f32_e32 v85, 0x42800000, v113
	v_mul_f32_e32 v13, 0x42800000, v111
	v_cvt_pk_fp8_f32 v82, v84, v85 op_sel:[0,0,1]
	v_mul_f32_e32 v84, 0x42800000, v109
	v_mov_b32_e32 v83, v3
	v_cvt_pk_fp8_f32 v83, v13, v84
	v_mul_f32_e32 v85, 0x42800000, v106
	v_mul_f32_e32 v86, 0x42800000, v102
	v_mul_f32_e32 v13, 0x42800000, v145
	v_cvt_pk_fp8_f32 v83, v85, v86 op_sel:[0,0,1]
	v_mul_f32_e32 v84, 0x42800000, v117
	v_mul_f32_e32 v85, 0x42800000, v101
	v_mul_f32_e32 v86, 0x42800000, v93
	ds_write_b128 v12, v[80:83] offset:32
	v_mul_f32_e32 v81, 0x42800000, v129
	v_mov_b32_e32 v80, v3
	v_cvt_pk_fp8_f32 v80, v13, v81
	v_mul_f32_e32 v82, 0x42800000, v127
	v_mul_f32_e32 v83, 0x42800000, v125
	v_mul_f32_e32 v13, 0x42800000, v123
	v_cvt_pk_fp8_f32 v80, v82, v83 op_sel:[0,0,1]
	v_mul_f32_e32 v82, 0x42800000, v122
	v_mov_b32_e32 v81, v3
	v_cvt_pk_fp8_f32 v81, v13, v82
	v_mul_f32_e32 v83, 0x42800000, v118
	v_mul_f32_e32 v13, 0x42800000, v108
	v_mov_b32_e32 v82, v3
	v_cvt_pk_fp8_f32 v81, v83, v84 op_sel:[0,0,1]
	v_mul_f32_e32 v83, 0x42800000, v107
	v_cvt_pk_fp8_f32 v82, v13, v83
	v_mul_f32_e32 v84, 0x42800000, v103
	v_mul_f32_e32 v13, 0x42800000, v98
	v_mov_b32_e32 v83, v3
	v_cvt_pk_fp8_f32 v82, v84, v85 op_sel:[0,0,1]
	v_mul_f32_e32 v84, 0x42800000, v96
	v_cvt_pk_fp8_f32 v83, v13, v84
	v_mul_f32_e32 v85, 0x42800000, v94
	v_mul_f32_e32 v13, 0x42800000, v188
	v_mul_f32_e32 v84, 0x42800000, v158
	v_cvt_pk_fp8_f32 v83, v85, v86 op_sel:[0,0,1]
	v_mul_f32_e32 v85, 0x42800000, v146
	v_mul_f32_e32 v15, 0x42800000, v15
	v_mul_f32_e32 v14, 0x42800000, v14
	ds_write_b128 v12, v[80:83] offset:48
	v_mul_f32_e32 v81, 0x42800000, v186
	v_mov_b32_e32 v80, v3
	v_cvt_pk_fp8_f32 v80, v13, v81
	v_mul_f32_e32 v82, 0x42800000, v183
	v_mul_f32_e32 v83, 0x42800000, v181
	v_mul_f32_e32 v13, 0x42800000, v170
	v_cvt_pk_fp8_f32 v80, v82, v83 op_sel:[0,0,1]
	v_mul_f32_e32 v82, 0x42800000, v167
	v_mov_b32_e32 v81, v3
	v_cvt_pk_fp8_f32 v81, v13, v82
	v_mul_f32_e32 v83, 0x42800000, v161
	v_mul_f32_e32 v13, 0x42800000, v153
	v_mov_b32_e32 v82, v3
	v_cvt_pk_fp8_f32 v81, v83, v84 op_sel:[0,0,1]
	v_mul_f32_e32 v83, 0x42800000, v150
	v_cvt_pk_fp8_f32 v82, v13, v83
	v_mul_f32_e32 v84, 0x42800000, v147
	v_mul_f32_e32 v13, 0x42800000, v144
	v_mov_b32_e32 v83, v3
	v_cvt_pk_fp8_f32 v82, v84, v85 op_sel:[0,0,1]
	v_mul_f32_e32 v84, 0x42800000, v143
	v_cvt_pk_fp8_f32 v83, v13, v84
	v_mul_f32_e32 v13, 0x42800000, v179
	v_mul_f32_e32 v84, 0x42800000, v148
	v_mul_f32_e32 v11, 0x42800000, v11
	v_cvt_pk_fp8_f32 v83, v15, v14 op_sel:[0,0,1]
	v_mul_f32_e32 v14, 0x42800000, v178
	v_mul_f32_e32 v15, 0x42800000, v175
	v_mul_f32_e32 v10, 0x42800000, v10
	ds_write_b128 v12, v[80:83] offset:64
	v_mov_b32_e32 v80, v3
	v_cvt_pk_fp8_f32 v80, v13, v14
	v_mul_f32_e32 v81, 0x42800000, v172
	v_mul_f32_e32 v13, 0x42800000, v168
	v_mul_f32_e32 v14, 0x42800000, v166
	v_cvt_pk_fp8_f32 v80, v15, v81 op_sel:[0,0,1]
	v_mov_b32_e32 v81, v3
	v_cvt_pk_fp8_f32 v81, v13, v14
	v_mul_f32_e32 v15, 0x42800000, v164
	v_mul_f32_e32 v82, 0x42800000, v162
	v_mul_f32_e32 v13, 0x42800000, v157
	v_cvt_pk_fp8_f32 v81, v15, v82 op_sel:[0,0,1]
	v_mul_f32_e32 v14, 0x42800000, v156
	v_mov_b32_e32 v82, v3
	v_cvt_pk_fp8_f32 v82, v13, v14
	v_mul_f32_e32 v15, 0x42800000, v155
	v_mul_f32_e32 v83, 0x42800000, v154
	v_mul_f32_e32 v13, 0x42800000, v152
	v_cvt_pk_fp8_f32 v82, v15, v83 op_sel:[0,0,1]
	v_mul_f32_e32 v14, 0x42800000, v151
	v_mov_b32_e32 v83, v3
	v_cvt_pk_fp8_f32 v83, v13, v14
	v_mul_f32_e32 v15, 0x42800000, v149
	v_mul_f32_e32 v13, 0x42800000, v203
	v_mul_f32_e32 v14, 0x42800000, v202
	v_cvt_pk_fp8_f32 v83, v15, v84 op_sel:[0,0,1]
	v_mul_f32_e32 v15, 0x42800000, v201
	v_mul_f32_e32 v84, 0x42800000, v173
	v_mul_f32_e32 v114, 0x42800000, v114
	ds_write_b128 v12, v[80:83] offset:80
	v_mov_b32_e32 v80, v3
	v_cvt_pk_fp8_f32 v80, v13, v14
	v_mul_f32_e32 v81, 0x42800000, v200
	v_mul_f32_e32 v13, 0x42800000, v199
	v_mul_f32_e32 v14, 0x42800000, v198
	v_cvt_pk_fp8_f32 v80, v15, v81 op_sel:[0,0,1]
	v_mov_b32_e32 v81, v3
	v_cvt_pk_fp8_f32 v81, v13, v14
	v_mul_f32_e32 v15, 0x42800000, v197
	v_mul_f32_e32 v82, 0x42800000, v196
	v_mul_f32_e32 v13, 0x42800000, v191
	v_cvt_pk_fp8_f32 v81, v15, v82 op_sel:[0,0,1]
	v_mul_f32_e32 v14, 0x42800000, v189
	v_mov_b32_e32 v82, v3
	v_cvt_pk_fp8_f32 v82, v13, v14
	v_mul_f32_e32 v15, 0x42800000, v185
	v_mul_f32_e32 v83, 0x42800000, v184
	v_mul_f32_e32 v13, 0x42800000, v182
	v_cvt_pk_fp8_f32 v82, v15, v83 op_sel:[0,0,1]
	v_mul_f32_e32 v14, 0x42800000, v180
	v_mov_b32_e32 v83, v3
	v_cvt_pk_fp8_f32 v83, v13, v14
	v_mul_f32_e32 v15, 0x42800000, v176
	v_mul_f32_e32 v13, 0x42800000, v195
	v_mul_f32_e32 v14, 0x42800000, v194
	v_cvt_pk_fp8_f32 v83, v15, v84 op_sel:[0,0,1]
	v_mul_f32_e32 v112, 0x42800000, v112
	v_mul_f32_e32 v97, 0x42800000, v97
	v_mul_f32_e32 v92, 0x42800000, v92
	ds_write_b128 v12, v[80:83] offset:96
	v_mov_b32_e32 v80, v3
	v_cvt_pk_fp8_f32 v80, v11, v10
	v_mul_f32_e32 v10, 0x42800000, v193
	v_mul_f32_e32 v11, 0x42800000, v192
	v_mov_b32_e32 v81, v3
	v_cvt_pk_fp8_f32 v81, v10, v11
	v_mul_f32_e32 v10, 0x42800000, v177
	v_mul_f32_e32 v11, 0x42800000, v174
	v_mov_b32_e32 v82, v3
	v_cvt_pk_fp8_f32 v82, v10, v11
	v_mul_f32_e32 v10, 0x42800000, v165
	v_mul_f32_e32 v11, 0x42800000, v163
	v_mov_b32_e32 v83, v3
	v_cvt_pk_fp8_f32 v83, v10, v11
	v_cvt_pk_fp8_f32 v80, v13, v14 op_sel:[0,0,1]
	v_mul_f32_e32 v13, 0x42800000, v190
	v_mul_f32_e32 v14, 0x42800000, v187
	v_cvt_pk_fp8_f32 v81, v13, v14 op_sel:[0,0,1]
	v_mul_f32_e32 v13, 0x42800000, v171
	v_mul_f32_e32 v14, 0x42800000, v169
	v_cvt_pk_fp8_f32 v82, v13, v14 op_sel:[0,0,1]
	v_mul_f32_e32 v13, 0x42800000, v160
	v_mul_f32_e32 v14, 0x42800000, v159
	v_cvt_pk_fp8_f32 v204, v114, v112 op_sel:[0,0,1]
	v_cvt_pk_fp8_f32 v205, v97, v92 op_sel:[0,0,1]
	v_cvt_pk_fp8_f32 v83, v13, v14 op_sel:[0,0,1]
	ds_write_b128 v12, v[204:207]
	ds_write_b128 v12, v[80:83] offset:112
	s_waitcnt lgkmcnt(0)
	v_add_u32_e32 v80, v19, v20
	v_lshl_add_u64 v[12:13], v[8:9], 0, v[4:5]
	ds_read_b128 v[8:11], v80
	v_lshl_add_u64 v[14:15], v[12:13], 0, v[2:3]
	v_or_b32_e32 v2, v79, v21
	v_lshlrev_b32_e32 v2, 10, v2
	s_waitcnt lgkmcnt(0)
	global_store_dwordx4 v[14:15], v[8:11], off
	ds_read_b128 v[8:11], v80 offset:1152
	v_lshl_add_u64 v[14:15], v[12:13], 0, v[2:3]
	v_or_b32_e32 v2, v79, v22
	v_lshlrev_b32_e32 v2, 10, v2
	s_waitcnt lgkmcnt(0)
	global_store_dwordx4 v[14:15], v[8:11], off
	ds_read_b128 v[8:11], v80 offset:2304
	v_lshl_add_u64 v[14:15], v[12:13], 0, v[2:3]
	v_or_b32_e32 v2, v79, v23
	v_lshlrev_b32_e32 v2, 10, v2
	s_waitcnt lgkmcnt(0)
	global_store_dwordx4 v[14:15], v[8:11], off
	ds_read_b128 v[8:11], v80 offset:3456
	v_lshl_add_u64 v[14:15], v[12:13], 0, v[2:3]
	v_or_b32_e32 v2, v79, v24
	v_lshlrev_b32_e32 v2, 10, v2
	s_waitcnt lgkmcnt(0)
	global_store_dwordx4 v[14:15], v[8:11], off
	ds_read_b128 v[8:11], v80 offset:4608
	v_lshl_add_u64 v[14:15], v[12:13], 0, v[2:3]
	v_or_b32_e32 v2, v79, v25
	v_lshlrev_b32_e32 v2, 10, v2
	s_waitcnt lgkmcnt(0)
	global_store_dwordx4 v[14:15], v[8:11], off
	ds_read_b128 v[8:11], v80 offset:5760
	v_lshl_add_u64 v[14:15], v[12:13], 0, v[2:3]
	v_or_b32_e32 v2, v79, v26
	v_lshlrev_b32_e32 v2, 10, v2
	s_waitcnt lgkmcnt(0)
	global_store_dwordx4 v[14:15], v[8:11], off
	ds_read_b128 v[8:11], v80 offset:6912
	v_lshl_add_u64 v[14:15], v[12:13], 0, v[2:3]
	v_or_b32_e32 v2, v79, v27
	v_lshlrev_b32_e32 v2, 10, v2
	v_lshl_add_u64 v[12:13], v[12:13], 0, v[2:3]
	s_waitcnt lgkmcnt(0)
	global_store_dwordx4 v[14:15], v[8:11], off
	ds_read_b128 v[8:11], v80 offset:8064
	s_waitcnt lgkmcnt(0)
	global_store_dwordx4 v[12:13], v[8:11], off
	s_waitcnt lgkmcnt(0)

.LBB0_789:
	s_or_b64 exec, exec, s[2:3]
	v_readlane_b32 s2, v253, 55
	s_waitcnt lgkmcnt(0)
	s_barrier
	v_mov_b32_e32 v0, s2
	v_readlane_b32 s2, v253, 54
	ds_read_b32 v0, v0
	s_nop 0
	v_mov_b32_e32 v1, s2
	ds_read_b32 v1, v1
	s_waitcnt lgkmcnt(0)
	s_barrier
	v_add_u32_e32 v201, 0x580, v0
	s_nop 0
	v_readfirstlane_b32 s100, v201
	v_readlane_b32 s101, v254, 38
	s_nop 3
	s_movk_i32 vcc_lo, 0x4c0
	s_movk_i32 vcc_hi, 0xe40
	s_cmp_eq_u32 s101, 0
	s_cselect_b32 vcc_lo, 0xac0, vcc_lo
	s_cselect_b32 vcc_hi, 0x1580, vcc_hi
	s_cmp_eq_u32 s101, 3
	s_cselect_b32 vcc_lo, 0, vcc_lo
	s_cselect_b32 vcc_hi, 0, vcc_hi
	s_add_i32 vcc_lo, s100, vcc_lo
	s_max_u32 vcc_lo, vcc_lo, vcc_hi
	v_mov_b32_e32 v201, vcc_lo
	v_readfirstlane_b32 s30, v0
	v_cmp_ge_i32_e32 vcc, v1, v201
	v_readfirstlane_b32 s24, v1
	s_cbranch_vccnz .LBB0_931
	s_add_u32 s31, s4, 0x37b00000
	s_addc_u32 s34, s5, 0
	s_add_i32 s35, s30, 0x480
	s_add_u32 s44, s4, 0x61800000
	s_addc_u32 s45, s5, 0
	s_add_u32 s46, s4, 0x42c00000
	s_addc_u32 s47, s5, 0
	s_add_u32 s10, s4, 0x66d00000
	s_addc_u32 s11, s5, 0
	s_add_u32 s48, s4, 0x61640000
	s_movk_i32 s2, 0x100
	s_addc_u32 s49, s5, 0
	v_cmp_gt_i32_e64 s[38:39], s2, v199
	s_add_i32 s2, 0, 0x14800
	v_add_u32_e32 v214, s2, v200
	s_add_i32 s2, 0, 0x16800
	s_cmp_lg_u32 0, -1
	v_lshlrev_b32_e32 v3, 1, v199
	v_lshlrev_b32_e32 v211, 4, v199
	s_cselect_b32 s3, 0, 0
	v_lshlrev_b32_e32 v0, 3, v199
	v_lshlrev_b32_e32 v1, 10, v101
	v_lshlrev_b32_e32 v2, 4, v198
	v_and_b32_e32 v3, 32, v3
	v_and_b32_e32 v5, 0xc0, v211
	s_addk_i32 s3, 0x6000
	v_and_b32_e32 v210, 24, v0
	v_lshl_or_b32 v5, v101, 8, v5
	v_add3_u32 v213, 0, v1, v2
	v_add_u32_e32 v1, s3, v3
	v_add3_u32 v217, v1, v210, v5
	v_lshrrev_b32_e32 v1, 3, v100
	v_lshl_add_u32 v215, v198, 2, s2
	v_and_b32_e32 v218, 56, v0
	v_lshl_add_u32 v220, v1, 2, s2
	s_add_i32 s2, 0, 0x14a00
	v_add_u32_e32 v4, 0, v3
	v_lshlrev_b32_e32 v96, 1, v218
	v_add_u32_e32 v221, s2, v200
	s_add_i32 s2, 0, 0x14900
	v_ashrrev_i32_e32 v203, 31, v202
	v_lshlrev_b32_e32 v208, 9, v100
	v_lshrrev_b32_e32 v209, 2, v100
	v_add3_u32 v212, v4, v210, v5
	v_cmp_gt_u32_e64 s[40:41], 32, v100
	v_cmp_lt_u32_e64 s[42:43], 31, v100
	v_or_b32_e32 v216, 0xc0, v206
	v_lshl_add_u64 v[204:205], s[4:5], 0, v[96:97]
	v_lshlrev_b32_e32 v219, 7, v1
	v_add_u32_e32 v222, s2, v200
	v_lshlrev_b32_e32 v96, 1, v98
	s_branch .LBB0_792

.LBB0_796:
	s_or_b64 exec, exec, s[2:3]
	v_readlane_b32 s101, v254, 38
	s_nop 3
	s_cmp_eq_u32 s101, 3
	s_cbranch_scc1 .Lc3_attn
	s_cmp_eq_u32 s101, 0
	s_cbranch_scc1 .Lc3_l0
	s_cmpk_lt_u32 s24, 0xe40
	s_cbranch_scc0 .Lc3_late
	s_mul_hi_u32 s101, s24, 0xaaaaaaab
	s_lshr_b32 s101, s101, 1
	s_mul_i32 s2, s101, 3
	s_sub_i32 s2, s24, s2
	s_cmp_eq_u32 s2, 2
	s_cbranch_scc1 .Lc3_entry
	s_sub_i32 s24, s24, s101
	s_branch .Lc3_chk
.Lc3_late:
	s_sub_i32 s24, s24, 0x4c0
	s_branch .Lc3_chk
.Lc3_l0:
	s_cmpk_lt_u32 s24, 0x1580
	s_cbranch_scc0 .Lc3_late0
	s_lshr_b32 s101, s24, 1
	s_bitcmp1_b32 s24, 0
	s_cbranch_scc1 .Lc3_entry
	s_sub_i32 s24, s24, s101
	s_branch .Lc3_chk
.Lc3_late0:
	s_sub_i32 s24, s24, 0xac0

.Lc3_entry:
	v_readlane_b32 s22, v252, 0
	v_readlane_b32 s23, v252, 1
	v_readlane_b32 s20, v254, 38
	s_lshr_b32 s2, s93, 6
	s_load_dwordx2 s[24:25], s[22:23], 0x98
	s_lshl_b32 s27, s2, 14
	s_add_i32 s20, s20, 1
	v_mbcnt_lo_u32_b32 v169, -1, 0
	v_mbcnt_hi_u32_b32 v169, -1, v169
	s_cmpk_lt_u32 s101, 0x4c0
	s_cbranch_scc1 .Lc3_nextl
	s_sub_i32 s101, s101, 0x4c0
	s_mov_b32 s20, 0
	s_lshl_b32 s19, s101, 3
	s_add_i32 s19, s19, s2
	s_branch .Lc3_have
.Lc3_nextl:
	s_lshl_b32 s19, s101, 3
	s_add_i32 s19, s19, s2
	s_addk_i32 s19, 0xa00
.Lc3_have:
	s_waitcnt lgkmcnt(0)
	s_cmpk_gt_i32 s19, 0x1fff
	v_lshrrev_b32_e32 v164, 4, v169
	v_and_b32_e32 v168, 15, v169
	v_lshrrev_b32_e32 v167, 3, v169
	s_cbranch_scc1 .Lc3_dn
	s_load_dwordx2 s[2:3], s[22:23], 0x60
	s_lshr_b32 s18, s19, 8
	s_lshl_b32 s21, s20, 5
	s_add_i32 s18, s18, s21
	s_bfe_u32 s21, s19, 0x30005
	s_and_b32 s26, s19, 31
	s_lshl_b32 s15, s18, 21
	s_add_u32 s12, s24, s15
	s_addc_u32 s13, s25, 0
	s_lshl_b32 s15, s21, 7
	s_add_i32 s15, s15, 0x3b00000
	s_lshr_b32 s14, s26, 2
	s_lshl_b32 s14, s14, 18
	s_add_i32 s15, s15, s14
	s_and_b32 s14, s26, 3
	s_lshl_b32 s14, s14, 15
	s_add_i32 s15, s15, s14
	s_add_u32 s12, s12, s15
	s_addc_u32 s13, s13, 0
	s_lshl_b32 s18, s18, 23
	s_lshl_b32 s21, s21, 20
	s_add_i32 s18, s18, s21
	s_lshl_b32 s26, s26, 8
	s_add_i32 s18, s18, s26
	s_waitcnt lgkmcnt(0)
	s_add_u32 s2, s2, s18
	s_addc_u32 s3, s3, 0
	s_movk_i32 s14, 0x2000
	s_movk_i32 s15, 0x1000
	s_mov_b32 s16, 0x42000000
	v_lshlrev_b32_e32 v164, 18, v164
	v_and_b32_e32 v166, 1, v167
	v_lshlrev_b32_e32 v166, 17, v166
	v_lshrrev_b32_e32 v167, 1, v167
	v_lshl_or_b32 v167, v167, 10, v166
	s_branch .Lc3_go
